# P6 gate/up GEMM epilogue: rows 2-7 token-scale loads hoisted into the first batch, vmcnt(0) drains replaced by counted waits
# speedup vs baseline: 1.0116x; 1.0116x over previous
.LBB0_511:
	s_lshl_b32 s1, s28, 2
	s_add_i32 s1, s1, 0
	s_add_i32 s1, s1, 0x20480
	v_mov_b32_e32 v42, s1
	ds_read_b32 v42, v42
	s_ashr_i32 s29, s28, 31
	v_lshl_or_b32 v169, s26, 7, v170
	s_lshl_b64 s[18:19], s[28:29], 13
	v_readlane_b32 s84, v252, 0
	s_waitcnt lgkmcnt(0)
	v_sub_u32_e32 v42, s56, v42
	v_lshl_add_u32 v184, v42, 8, v189
	v_readlane_b32 s85, v252, 1
	s_add_u32 s22, s84, s18
	v_lshlrev_b32_e32 v42, 1, v169
	s_addc_u32 s23, s85, s19
	v_ashrrev_i32_e32 v43, 31, v42
	v_lshl_add_u64 v[50:51], v[42:43], 2, s[22:23]
	global_load_dwordx4 v[42:45], v[50:51], off offset:48
	global_load_dwordx4 v[46:49], v[50:51], off offset:32
	global_load_dwordx4 v[66:69], v[50:51], off offset:16
	global_load_dwordx4 v[70:73], v[50:51], off
	s_add_u32 s1, s46, s18
	s_addc_u32 s21, s47, s19
	s_lshl_b32 s18, s26, 8
	s_ashr_i32 s19, s18, 31
	s_lshl_b64 s[18:19], s[18:19], 2
	s_add_u32 s18, s1, s18
	s_addc_u32 s19, s21, s19
	v_ashrrev_i32_e32 v185, 31, v184
	v_cvt_f32_i32_e32 v151, v151
	v_cvt_f32_i32_e32 v150, v150
	v_cvt_f32_i32_e32 v159, v159
	v_cvt_f32_i32_e32 v158, v158
	v_cvt_f32_i32_e32 v147, v147
	v_cvt_f32_i32_e32 v146, v146
	v_cvt_f32_i32_e32 v155, v155
	v_cvt_f32_i32_e32 v154, v154
	v_cvt_f32_i32_e32 v149, v149
	v_cvt_f32_i32_e32 v148, v148
	v_cvt_f32_i32_e32 v157, v157
	v_cvt_f32_i32_e32 v156, v156
	v_cvt_f32_i32_e32 v131, v131
	v_cvt_f32_i32_e32 v130, v130
	v_cvt_f32_i32_e32 v133, v133
	v_cvt_f32_i32_e32 v132, v132
	v_sub_u32_e32 v172, v169, v190
	v_ashrrev_i32_e32 v173, 31, v172
	v_cvt_f32_i32_e32 v115, v115
	v_cvt_f32_i32_e32 v114, v114
	v_cvt_f32_i32_e32 v117, v117
	v_cvt_f32_i32_e32 v116, v116
	v_cvt_f32_i32_e32 v99, v99
	v_cvt_f32_i32_e32 v98, v98
	v_cvt_f32_i32_e32 v101, v101
	v_cvt_f32_i32_e32 v100, v100
	v_cvt_f32_i32_e32 v83, v83
	v_cvt_f32_i32_e32 v82, v82
	v_cvt_f32_i32_e32 v85, v85
	v_cvt_f32_i32_e32 v84, v84
	v_cvt_f32_i32_e32 v59, v59
	v_cvt_f32_i32_e32 v58, v58
	v_cvt_f32_i32_e32 v61, v61
	v_cvt_f32_i32_e32 v60, v60
	v_cvt_f32_i32_e32 v39, v39
	v_cvt_f32_i32_e32 v38, v38
	v_cvt_f32_i32_e32 v23, v23
	v_cvt_f32_i32_e32 v22, v22
	v_cvt_f32_i32_e32 v25, v25
	v_cvt_f32_i32_e32 v24, v24
	v_cvt_f32_i32_e32 v19, v19
	v_cvt_f32_i32_e32 v18, v18
	v_cvt_f32_i32_e32 v11, v11
	v_cvt_f32_i32_e32 v10, v10
	v_cvt_f32_i32_e32 v15, v15
	v_cvt_f32_i32_e32 v14, v14
	v_cvt_f32_i32_e32 v13, v13
	v_cvt_f32_i32_e32 v12, v12
	v_cvt_f32_i32_e32 v3, v3
	v_cvt_f32_i32_e32 v2, v2
	v_cvt_f32_i32_e32 v7, v7
	v_cvt_f32_i32_e32 v6, v6
	v_cvt_f32_i32_e32 v5, v5
	v_cvt_f32_i32_e32 v4, v4
	v_readlane_b32 s86, v252, 2
	v_readlane_b32 s87, v252, 3
	v_readlane_b32 s88, v252, 4
	v_readlane_b32 s89, v252, 5
	v_readlane_b32 s90, v252, 6
	v_readlane_b32 s91, v252, 7
	s_waitcnt vmcnt(0)
	v_mov_b32_e32 v50, v67
	v_mov_b32_e32 v51, v69
	v_pk_add_f32 v[180:181], v[50:51], 1.0 op_sel_hi:[1,0]
	v_mov_b32_e32 v50, v71
	v_mov_b32_e32 v51, v73
	v_pk_add_f32 v[182:183], v[50:51], 1.0 op_sel_hi:[1,0]
	v_mov_b32_e32 v50, v43
	v_mov_b32_e32 v51, v45
	v_pk_add_f32 v[176:177], v[50:51], 1.0 op_sel_hi:[1,0]
	v_mov_b32_e32 v50, v47
	v_mov_b32_e32 v51, v49
	v_lshlrev_b32_e32 v43, 2, v170
	v_pk_add_f32 v[178:179], v[50:51], 1.0 op_sel_hi:[1,0]
	global_load_dwordx4 v[50:53], v43, s[18:19] offset:16
	global_load_dwordx4 v[74:77], v43, s[18:19]
	global_load_dwordx4 v[54:57], v43, s[18:19] offset:528
	global_load_dwordx4 v[78:81], v43, s[18:19] offset:512
	s_lshl_b64 s[18:19], s[28:29], 18
	s_add_u32 s18, s66, s18
	s_addc_u32 s19, s67, s19
	v_lshl_add_u64 v[184:185], v[184:185], 2, s[18:19]
	global_load_dword v212, v[184:185], off
	v_mov_b32_e32 v43, v44
	global_load_dword v44, v[184:185], off offset:64
	global_load_dword v220, v[184:185], off offset:128
	global_load_dword v222, v[184:185], off offset:192
	global_load_dword v224, v[184:185], off offset:512
	global_load_dword v226, v[184:185], off offset:576
	global_load_dword v228, v[184:185], off offset:640
	global_load_dword v230, v[184:185], off offset:704
	v_mov_b32_e32 v47, v48
	v_mov_b32_e32 v71, v72
	v_mov_b32_e32 v67, v68
	v_lshl_add_u32 v45, s56, 8, v189
	s_mov_b64 s[18:19], -1
	s_and_b64 vcc, exec, s[2:3]
	s_waitcnt vmcnt(11)
	v_pk_mul_f32 v[48:49], v[50:51], v[150:151]
	s_waitcnt vmcnt(10)
	v_pk_mul_f32 v[72:73], v[74:75], v[158:159]
	s_waitcnt vmcnt(9)
	v_pk_mul_f32 v[146:147], v[54:55], v[146:147]
	s_waitcnt vmcnt(8)
	v_pk_mul_f32 v[154:155], v[78:79], v[154:155]
	v_pk_mul_f32 v[148:149], v[56:57], v[148:149]
	v_pk_mul_f32 v[130:131], v[54:55], v[130:131]
	v_pk_mul_f32 v[132:133], v[56:57], v[132:133]
	v_pk_mul_f32 v[114:115], v[54:55], v[114:115]
	s_waitcnt vmcnt(7)
	v_pk_fma_f32 v[48:49], v[48:49], v[212:213], v[46:47] op_sel_hi:[1,0,1]
	v_pk_fma_f32 v[72:73], v[72:73], v[212:213], v[70:71] op_sel_hi:[1,0,1]
	v_min_f32_e32 v48, 0x40e00000, v48
	v_min_f32_e32 v49, 0x40e00000, v49
	v_pk_mul_f32 v[150:151], v[48:49], s[12:13] op_sel_hi:[1,0]
	v_pk_fma_f32 v[146:147], v[146:147], v[212:213], v[178:179] op_sel_hi:[1,0,1]
	v_exp_f32_e32 v150, v150
	v_exp_f32_e32 v151, v151
	v_min_f32_e32 v72, 0x40e00000, v72
	v_min_f32_e32 v73, 0x40e00000, v73
	v_med3_f32 v146, v146, s54, v210
	v_pk_fma_f32 v[150:151], v[150:151], s[14:15], s[14:15] op_sel_hi:[1,0,0]
	v_med3_f32 v147, v147, s54, v210
	v_rcp_f32_e32 v150, v150
	v_rcp_f32_e32 v151, v151
	v_pk_mul_f32 v[158:159], v[72:73], s[12:13] op_sel_hi:[1,0]
	v_pk_fma_f32 v[154:155], v[154:155], v[212:213], v[182:183] op_sel_hi:[1,0,1]
	v_exp_f32_e32 v158, v158
	v_pk_mul_f32 v[48:49], v[48:49], v[150:151]
	v_exp_f32_e32 v159, v159
	v_pk_mul_f32 v[48:49], v[146:147], v[48:49]
	v_cvt_f32_i32_e32 v147, v153
	v_cvt_f32_i32_e32 v146, v152
	v_pk_fma_f32 v[158:159], v[158:159], s[14:15], s[14:15] op_sel_hi:[1,0,0]
	v_med3_f32 v154, v154, s54, v210
	v_rcp_f32_e32 v158, v158
	v_pk_mul_f32 v[146:147], v[52:53], v[146:147]
	v_rcp_f32_e32 v159, v159
	v_pk_fma_f32 v[146:147], v[146:147], v[212:213], v[42:43] op_sel_hi:[1,0,1]
	v_med3_f32 v155, v155, s54, v210
	v_min_f32_e32 v146, 0x40e00000, v146
	v_min_f32_e32 v147, 0x40e00000, v147
	v_pk_mul_f32 v[150:151], v[146:147], s[12:13] op_sel_hi:[1,0]
	v_pk_mul_f32 v[72:73], v[72:73], v[158:159]
	v_exp_f32_e32 v150, v150
	v_exp_f32_e32 v151, v151
	v_pk_mul_f32 v[72:73], v[154:155], v[72:73]
	v_cvt_f32_i32_e32 v155, v161
	v_cvt_f32_i32_e32 v154, v160
	v_pk_fma_f32 v[150:151], v[150:151], s[14:15], s[14:15] op_sel_hi:[1,0,0]
	v_pk_fma_f32 v[148:149], v[148:149], v[212:213], v[176:177] op_sel_hi:[1,0,1]
	v_rcp_f32_e32 v150, v150
	v_rcp_f32_e32 v151, v151
	v_pk_mul_f32 v[68:69], v[76:77], v[154:155]
	v_med3_f32 v148, v148, s54, v210
	v_pk_fma_f32 v[68:69], v[68:69], v[212:213], v[66:67] op_sel_hi:[1,0,1]
	v_med3_f32 v149, v149, s54, v210
	v_min_f32_e32 v68, 0x40e00000, v68
	v_min_f32_e32 v69, 0x40e00000, v69
	v_pk_mul_f32 v[146:147], v[146:147], v[150:151]
	v_pk_mul_f32 v[154:155], v[80:81], v[156:157]
	v_pk_mul_f32 v[156:157], v[68:69], s[12:13] op_sel_hi:[1,0]
	v_pk_mul_f32 v[148:149], v[148:149], v[146:147]
	v_mov_b32_e32 v147, v167
	v_exp_f32_e32 v156, v156
	v_exp_f32_e32 v157, v157
	v_cvt_pk_fp8_f32 v147, v48, v49
	v_cvt_f32_i32_e32 v49, v143
	v_cvt_f32_i32_e32 v48, v142
	v_pk_fma_f32 v[156:157], v[156:157], s[14:15], s[14:15] op_sel_hi:[1,0,0]
	v_mov_b32_e32 v146, v167
	v_rcp_f32_e32 v156, v156
	v_pk_mul_f32 v[48:49], v[74:75], v[48:49]
	v_rcp_f32_e32 v157, v157
	s_waitcnt vmcnt(6)
	v_pk_fma_f32 v[48:49], v[48:49], v[44:45], v[70:71] op_sel_hi:[1,0,1]
	v_cvt_pk_fp8_f32 v146, v72, v73
	v_min_f32_e32 v48, 0x40e00000, v48
	v_min_f32_e32 v49, 0x40e00000, v49
	v_pk_mul_f32 v[72:73], v[48:49], s[12:13] op_sel_hi:[1,0]
	v_pk_fma_f32 v[154:155], v[154:155], v[212:213], v[180:181] op_sel_hi:[1,0,1]
	v_exp_f32_e32 v72, v72
	v_exp_f32_e32 v73, v73
	v_med3_f32 v154, v154, s54, v210
	v_med3_f32 v155, v155, s54, v210
	v_pk_mul_f32 v[68:69], v[68:69], v[156:157]
	v_pk_fma_f32 v[72:73], v[72:73], s[14:15], s[14:15] op_sel_hi:[1,0,0]
	v_pk_mul_f32 v[68:69], v[154:155], v[68:69]
	v_rcp_f32_e32 v72, v72
	v_cvt_pk_fp8_f32 v146, v68, v69 op_sel:[0,0,1]
	v_cvt_f32_i32_e32 v69, v139
	v_cvt_f32_i32_e32 v68, v138
	v_rcp_f32_e32 v73, v73
	v_pk_fma_f32 v[130:131], v[130:131], v[44:45], v[178:179] op_sel_hi:[1,0,1]
	v_cvt_pk_fp8_f32 v147, v148, v149 op_sel:[0,0,1]
	v_pk_mul_f32 v[68:69], v[78:79], v[68:69]
	v_pk_mul_f32 v[48:49], v[48:49], v[72:73]
	v_pk_fma_f32 v[68:69], v[68:69], v[44:45], v[182:183] op_sel_hi:[1,0,1]
	v_cvt_f32_i32_e32 v73, v141
	v_med3_f32 v68, v68, s54, v210
	v_med3_f32 v69, v69, s54, v210
	v_pk_mul_f32 v[48:49], v[68:69], v[48:49]
	v_cvt_f32_i32_e32 v69, v145
	v_cvt_f32_i32_e32 v68, v144
	v_cvt_f32_i32_e32 v72, v140
	v_med3_f32 v130, v130, s54, v210
	v_med3_f32 v131, v131, s54, v210
	v_pk_mul_f32 v[68:69], v[76:77], v[68:69]
	v_pk_mul_f32 v[72:73], v[80:81], v[72:73]
	v_pk_fma_f32 v[68:69], v[68:69], v[44:45], v[66:67] op_sel_hi:[1,0,1]
	v_pk_fma_f32 v[72:73], v[72:73], v[44:45], v[180:181] op_sel_hi:[1,0,1]
	v_min_f32_e32 v68, 0x40e00000, v68
	v_min_f32_e32 v69, 0x40e00000, v69
	v_pk_mul_f32 v[138:139], v[68:69], s[12:13] op_sel_hi:[1,0]
	v_med3_f32 v72, v72, s54, v210
	v_exp_f32_e32 v138, v138
	v_exp_f32_e32 v139, v139
	v_med3_f32 v73, v73, s54, v210
	v_mov_b32_e32 v148, v167
	v_mov_b32_e32 v149, v167
	v_pk_fma_f32 v[138:139], v[138:139], s[14:15], s[14:15] op_sel_hi:[1,0,0]
	v_cvt_pk_fp8_f32 v148, v48, v49
	v_rcp_f32_e32 v138, v138
	v_rcp_f32_e32 v139, v139
	v_pk_fma_f32 v[132:133], v[132:133], v[44:45], v[176:177] op_sel_hi:[1,0,1]
	v_or_b32_e32 v48, v45, v191
	v_med3_f32 v132, v132, s54, v210
	v_pk_mul_f32 v[68:69], v[68:69], v[138:139]
	v_med3_f32 v133, v133, s54, v210
	v_pk_mul_f32 v[68:69], v[72:73], v[68:69]
	v_cvt_f32_i32_e32 v73, v135
	v_cvt_f32_i32_e32 v72, v134
	v_cvt_pk_fp8_f32 v148, v68, v69 op_sel:[0,0,1]
	v_ashrrev_i32_e32 v49, 31, v48
	v_lshlrev_b64 v[48:49], 10, v[48:49]
	v_pk_mul_f32 v[72:73], v[50:51], v[72:73]
	v_lshl_add_u64 v[48:49], s[94:95], 0, v[48:49]
	v_pk_fma_f32 v[72:73], v[72:73], v[44:45], v[46:47] op_sel_hi:[1,0,1]
	v_permlane16_swap_b32_e32 v146, v148
	v_min_f32_e32 v72, 0x40e00000, v72
	v_min_f32_e32 v73, 0x40e00000, v73
	v_pk_mul_f32 v[134:135], v[72:73], s[12:13] op_sel_hi:[1,0]
	v_lshl_add_u64 v[48:49], v[48:49], 0, v[172:173]
	v_exp_f32_e32 v134, v134
	v_exp_f32_e32 v135, v135
	v_cvt_f32_i32_e32 v69, v123
	v_cvt_f32_i32_e32 v68, v122
	v_pk_mul_f32 v[116:117], v[56:57], v[116:117]
	v_pk_fma_f32 v[134:135], v[134:135], s[14:15], s[14:15] op_sel_hi:[1,0,0]
	v_pk_mul_f32 v[98:99], v[54:55], v[98:99]
	v_rcp_f32_e32 v134, v134
	v_rcp_f32_e32 v135, v135
	v_pk_mul_f32 v[68:69], v[78:79], v[68:69]
	v_pk_mul_f32 v[100:101], v[56:57], v[100:101]
	v_pk_mul_f32 v[82:83], v[54:55], v[82:83]
	v_pk_mul_f32 v[72:73], v[72:73], v[134:135]
	v_pk_mul_f32 v[84:85], v[56:57], v[84:85]
	v_pk_mul_f32 v[72:73], v[130:131], v[72:73]
	v_cvt_f32_i32_e32 v131, v137
	v_cvt_f32_i32_e32 v130, v136
	v_cvt_pk_fp8_f32 v149, v72, v73
	v_pk_mul_f32 v[58:59], v[78:79], v[58:59]
	v_pk_mul_f32 v[60:61], v[80:81], v[60:61]
	v_pk_mul_f32 v[130:131], v[52:53], v[130:131]
	v_pk_mul_f32 v[38:39], v[50:51], v[38:39]
	v_pk_fma_f32 v[130:131], v[130:131], v[44:45], v[42:43] op_sel_hi:[1,0,1]
	v_pk_mul_f32 v[22:23], v[54:55], v[22:23]
	v_min_f32_e32 v130, 0x40e00000, v130
	v_min_f32_e32 v131, 0x40e00000, v131
	v_pk_mul_f32 v[134:135], v[130:131], s[12:13] op_sel_hi:[1,0]
	v_pk_mul_f32 v[24:25], v[56:57], v[24:25]
	v_exp_f32_e32 v134, v134
	v_exp_f32_e32 v135, v135
	v_pk_mul_f32 v[18:19], v[50:51], v[18:19]
	v_pk_mul_f32 v[10:11], v[74:75], v[10:11]
	v_pk_mul_f32 v[14:15], v[78:79], v[14:15]
	v_pk_fma_f32 v[134:135], v[134:135], s[14:15], s[14:15] op_sel_hi:[1,0,0]
	v_pk_mul_f32 v[12:13], v[76:77], v[12:13]
	v_rcp_f32_e32 v134, v134
	v_rcp_f32_e32 v135, v135
	v_pk_mul_f32 v[2:3], v[50:51], v[2:3]
	v_pk_mul_f32 v[6:7], v[54:55], v[6:7]
	v_pk_mul_f32 v[4:5], v[52:53], v[4:5]
	v_pk_mul_f32 v[130:131], v[130:131], v[134:135]
	s_nop 0
	v_pk_mul_f32 v[130:131], v[132:133], v[130:131]
	s_nop 0
	v_cvt_pk_fp8_f32 v149, v130, v131 op_sel:[0,0,1]
	s_nop 1
	v_permlane16_swap_b32_e32 v147, v149
	global_store_dwordx4 v[48:49], v[146:149], off
	s_nop 0
	v_cvt_f32_i32_e32 v49, v127
	v_cvt_f32_i32_e32 v48, v126
	v_pk_mul_f32 v[48:49], v[74:75], v[48:49]
	s_waitcnt vmcnt(6)
	v_pk_fma_f32 v[48:49], v[48:49], v[220:221], v[70:71] op_sel_hi:[1,0,1]
	s_nop 0
	v_min_f32_e32 v48, 0x40e00000, v48
	v_min_f32_e32 v49, 0x40e00000, v49
	v_pk_mul_f32 v[72:73], v[48:49], s[12:13] op_sel_hi:[1,0]
	v_pk_fma_f32 v[68:69], v[68:69], v[220:221], v[182:183] op_sel_hi:[1,0,1]
	v_exp_f32_e32 v72, v72
	v_exp_f32_e32 v73, v73
	v_med3_f32 v68, v68, s54, v210
	v_med3_f32 v69, v69, s54, v210
	v_pk_fma_f32 v[114:115], v[114:115], v[220:221], v[178:179] op_sel_hi:[1,0,1]
	v_pk_fma_f32 v[72:73], v[72:73], s[14:15], s[14:15] op_sel_hi:[1,0,0]
	v_med3_f32 v114, v114, s54, v210
	v_rcp_f32_e32 v72, v72
	v_rcp_f32_e32 v73, v73
	v_med3_f32 v115, v115, s54, v210
	v_pk_fma_f32 v[116:117], v[116:117], v[220:221], v[176:177] op_sel_hi:[1,0,1]
	v_pk_mul_f32 v[48:49], v[48:49], v[72:73]
	s_nop 0
	v_pk_mul_f32 v[48:49], v[68:69], v[48:49]
	v_cvt_f32_i32_e32 v69, v129
	v_cvt_f32_i32_e32 v68, v128
	v_cvt_f32_i32_e32 v73, v125
	v_cvt_f32_i32_e32 v72, v124
	v_med3_f32 v116, v116, s54, v210
	v_pk_mul_f32 v[68:69], v[76:77], v[68:69]
	v_med3_f32 v117, v117, s54, v210
	v_pk_fma_f32 v[68:69], v[68:69], v[220:221], v[66:67] op_sel_hi:[1,0,1]
	v_pk_mul_f32 v[72:73], v[80:81], v[72:73]
	v_min_f32_e32 v68, 0x40e00000, v68
	v_min_f32_e32 v69, 0x40e00000, v69
	v_pk_mul_f32 v[122:123], v[68:69], s[12:13] op_sel_hi:[1,0]
	v_pk_fma_f32 v[72:73], v[72:73], v[220:221], v[180:181] op_sel_hi:[1,0,1]
	v_exp_f32_e32 v122, v122
	v_exp_f32_e32 v123, v123
	v_med3_f32 v72, v72, s54, v210
	v_med3_f32 v73, v73, s54, v210
	v_pk_fma_f32 v[122:123], v[122:123], s[14:15], s[14:15] op_sel_hi:[1,0,0]
	s_nop 0
	v_rcp_f32_e32 v122, v122
	v_rcp_f32_e32 v123, v123
	s_nop 0
	v_pk_mul_f32 v[68:69], v[68:69], v[122:123]
	s_nop 0
	v_pk_mul_f32 v[68:69], v[72:73], v[68:69]
	v_cvt_f32_i32_e32 v73, v119
	v_cvt_f32_i32_e32 v72, v118
	v_pk_mul_f32 v[72:73], v[50:51], v[72:73]
	s_nop 0
	v_pk_fma_f32 v[72:73], v[72:73], v[220:221], v[46:47] op_sel_hi:[1,0,1]
	s_nop 0
	v_min_f32_e32 v72, 0x40e00000, v72
	v_min_f32_e32 v73, 0x40e00000, v73
	v_pk_mul_f32 v[118:119], v[72:73], s[12:13] op_sel_hi:[1,0]
	s_nop 0
	v_exp_f32_e32 v118, v118
	v_exp_f32_e32 v119, v119
	s_nop 0
	v_pk_fma_f32 v[118:119], v[118:119], s[14:15], s[14:15] op_sel_hi:[1,0,0]
	s_nop 0
	v_rcp_f32_e32 v118, v118
	v_rcp_f32_e32 v119, v119
	s_nop 0
	v_pk_mul_f32 v[72:73], v[72:73], v[118:119]
	s_nop 0
	v_pk_mul_f32 v[72:73], v[114:115], v[72:73]
	v_cvt_f32_i32_e32 v115, v121
	v_cvt_f32_i32_e32 v114, v120
	v_pk_mul_f32 v[114:115], v[52:53], v[114:115]
	s_nop 0
	v_pk_fma_f32 v[114:115], v[114:115], v[220:221], v[42:43] op_sel_hi:[1,0,1]
	s_nop 0
	v_min_f32_e32 v114, 0x40e00000, v114
	v_min_f32_e32 v115, 0x40e00000, v115
	v_pk_mul_f32 v[118:119], v[114:115], s[12:13] op_sel_hi:[1,0]
	s_waitcnt vmcnt(5)
	v_pk_fma_f32 v[98:99], v[98:99], v[222:223], v[178:179] op_sel_hi:[1,0,1]
	v_exp_f32_e32 v118, v118
	v_exp_f32_e32 v119, v119
	v_med3_f32 v98, v98, s54, v210
	v_med3_f32 v99, v99, s54, v210
	v_pk_fma_f32 v[100:101], v[100:101], v[222:223], v[176:177] op_sel_hi:[1,0,1]
	v_pk_fma_f32 v[118:119], v[118:119], s[14:15], s[14:15] op_sel_hi:[1,0,0]
	v_med3_f32 v100, v100, s54, v210
	v_rcp_f32_e32 v118, v118
	v_rcp_f32_e32 v119, v119
	v_med3_f32 v101, v101, s54, v210
	v_pk_mul_f32 v[114:115], v[114:115], v[118:119]
	s_nop 0
	v_pk_mul_f32 v[116:117], v[116:117], v[114:115]
	v_mov_b32_e32 v114, v167
	v_cvt_pk_fp8_f32 v114, v48, v49
	v_cvt_f32_i32_e32 v49, v111
	v_cvt_f32_i32_e32 v48, v110
	v_mov_b32_e32 v115, v167
	v_cvt_pk_fp8_f32 v115, v72, v73
	v_cvt_pk_fp8_f32 v114, v68, v69 op_sel:[0,0,1]
	v_pk_mul_f32 v[48:49], v[74:75], v[48:49]
	v_cvt_f32_i32_e32 v69, v107
	v_pk_fma_f32 v[48:49], v[48:49], v[222:223], v[70:71] op_sel_hi:[1,0,1]
	v_cvt_f32_i32_e32 v68, v106
	v_min_f32_e32 v48, 0x40e00000, v48
	v_min_f32_e32 v49, 0x40e00000, v49
	v_pk_mul_f32 v[72:73], v[48:49], s[12:13] op_sel_hi:[1,0]
	v_pk_mul_f32 v[68:69], v[78:79], v[68:69]
	v_exp_f32_e32 v72, v72
	v_exp_f32_e32 v73, v73
	v_pk_fma_f32 v[68:69], v[68:69], v[222:223], v[182:183] op_sel_hi:[1,0,1]
	v_cvt_pk_fp8_f32 v115, v116, v117 op_sel:[0,0,1]
	v_med3_f32 v68, v68, s54, v210
	v_pk_fma_f32 v[72:73], v[72:73], s[14:15], s[14:15] op_sel_hi:[1,0,0]
	v_med3_f32 v69, v69, s54, v210
	v_rcp_f32_e32 v72, v72
	v_rcp_f32_e32 v73, v73
	v_mov_b32_e32 v116, v167
	v_mov_b32_e32 v117, v167
	v_pk_mul_f32 v[48:49], v[48:49], v[72:73]
	s_nop 0
	v_pk_mul_f32 v[48:49], v[68:69], v[48:49]
	v_cvt_f32_i32_e32 v69, v113
	v_cvt_f32_i32_e32 v68, v112
	v_cvt_f32_i32_e32 v73, v109
	v_cvt_f32_i32_e32 v72, v108
	v_cvt_pk_fp8_f32 v116, v48, v49
	v_pk_mul_f32 v[68:69], v[76:77], v[68:69]
	v_or_b32_e32 v48, v45, v192
	v_pk_fma_f32 v[68:69], v[68:69], v[222:223], v[66:67] op_sel_hi:[1,0,1]
	v_pk_mul_f32 v[72:73], v[80:81], v[72:73]
	v_min_f32_e32 v68, 0x40e00000, v68
	v_min_f32_e32 v69, 0x40e00000, v69
	v_pk_mul_f32 v[106:107], v[68:69], s[12:13] op_sel_hi:[1,0]
	v_pk_fma_f32 v[72:73], v[72:73], v[222:223], v[180:181] op_sel_hi:[1,0,1]
	v_exp_f32_e32 v106, v106
	v_exp_f32_e32 v107, v107
	v_med3_f32 v72, v72, s54, v210
	v_med3_f32 v73, v73, s54, v210
	v_ashrrev_i32_e32 v49, 31, v48
	v_pk_fma_f32 v[106:107], v[106:107], s[14:15], s[14:15] op_sel_hi:[1,0,0]
	v_lshlrev_b64 v[48:49], 10, v[48:49]
	v_rcp_f32_e32 v106, v106
	v_rcp_f32_e32 v107, v107
	v_lshl_add_u64 v[48:49], s[94:95], 0, v[48:49]
	v_lshl_add_u64 v[48:49], v[48:49], 0, v[172:173]
	v_pk_mul_f32 v[68:69], v[68:69], v[106:107]
	s_nop 0
	v_pk_mul_f32 v[68:69], v[72:73], v[68:69]
	v_cvt_f32_i32_e32 v73, v103
	v_cvt_f32_i32_e32 v72, v102
	v_cvt_pk_fp8_f32 v116, v68, v69 op_sel:[0,0,1]
	v_cvt_f32_i32_e32 v69, v91
	v_cvt_f32_i32_e32 v68, v90
	v_pk_mul_f32 v[72:73], v[50:51], v[72:73]
	v_permlane16_swap_b32_e32 v114, v116
	v_pk_fma_f32 v[72:73], v[72:73], v[222:223], v[46:47] op_sel_hi:[1,0,1]
	v_pk_mul_f32 v[68:69], v[78:79], v[68:69]
	v_min_f32_e32 v72, 0x40e00000, v72
	v_min_f32_e32 v73, 0x40e00000, v73
	v_pk_mul_f32 v[102:103], v[72:73], s[12:13] op_sel_hi:[1,0]
	s_nop 0
	v_exp_f32_e32 v102, v102
	v_exp_f32_e32 v103, v103
	s_nop 0
	v_pk_fma_f32 v[102:103], v[102:103], s[14:15], s[14:15] op_sel_hi:[1,0,0]
	s_nop 0
	v_rcp_f32_e32 v102, v102
	v_rcp_f32_e32 v103, v103
	s_nop 0
	v_pk_mul_f32 v[72:73], v[72:73], v[102:103]
	s_nop 0
	v_pk_mul_f32 v[72:73], v[98:99], v[72:73]
	v_cvt_f32_i32_e32 v99, v105
	v_cvt_f32_i32_e32 v98, v104
	v_cvt_pk_fp8_f32 v117, v72, v73
	v_pk_mul_f32 v[98:99], v[52:53], v[98:99]
	s_nop 0
	v_pk_fma_f32 v[98:99], v[98:99], v[222:223], v[42:43] op_sel_hi:[1,0,1]
	v_add_u32_e32 v45, 0x80, v45
	v_min_f32_e32 v98, 0x40e00000, v98
	v_min_f32_e32 v99, 0x40e00000, v99
	v_pk_mul_f32 v[102:103], v[98:99], s[12:13] op_sel_hi:[1,0]
	s_nop 0
	v_exp_f32_e32 v102, v102
	v_exp_f32_e32 v103, v103
	s_nop 0
	v_pk_fma_f32 v[102:103], v[102:103], s[14:15], s[14:15] op_sel_hi:[1,0,0]
	s_nop 0
	v_rcp_f32_e32 v102, v102
	v_rcp_f32_e32 v103, v103
	s_nop 0
	v_pk_mul_f32 v[98:99], v[98:99], v[102:103]
	s_nop 0
	v_pk_mul_f32 v[98:99], v[100:101], v[98:99]
	s_nop 0
	v_cvt_pk_fp8_f32 v117, v98, v99 op_sel:[0,0,1]
	s_nop 1
	v_permlane16_swap_b32_e32 v115, v117
	global_store_dwordx4 v[48:49], v[114:117], off
	s_nop 0
	v_cvt_f32_i32_e32 v49, v95
	v_cvt_f32_i32_e32 v48, v94
	v_pk_mul_f32 v[48:49], v[74:75], v[48:49]
	s_waitcnt vmcnt(5)
	v_pk_fma_f32 v[48:49], v[48:49], v[224:225], v[70:71] op_sel_hi:[1,0,1]
	s_nop 0
	v_min_f32_e32 v48, 0x40e00000, v48
	v_min_f32_e32 v49, 0x40e00000, v49
	v_pk_mul_f32 v[72:73], v[48:49], s[12:13] op_sel_hi:[1,0]
	v_pk_fma_f32 v[68:69], v[68:69], v[224:225], v[182:183] op_sel_hi:[1,0,1]
	v_exp_f32_e32 v72, v72
	v_exp_f32_e32 v73, v73
	v_med3_f32 v68, v68, s54, v210
	v_med3_f32 v69, v69, s54, v210
	v_pk_fma_f32 v[82:83], v[82:83], v[224:225], v[178:179] op_sel_hi:[1,0,1]
	v_pk_fma_f32 v[72:73], v[72:73], s[14:15], s[14:15] op_sel_hi:[1,0,0]
	v_med3_f32 v82, v82, s54, v210
	v_rcp_f32_e32 v72, v72
	v_rcp_f32_e32 v73, v73
	v_med3_f32 v83, v83, s54, v210
	v_pk_fma_f32 v[84:85], v[84:85], v[224:225], v[176:177] op_sel_hi:[1,0,1]
	v_pk_mul_f32 v[48:49], v[48:49], v[72:73]
	s_nop 0
	v_pk_mul_f32 v[48:49], v[68:69], v[48:49]
	v_cvt_f32_i32_e32 v69, v97
	v_cvt_f32_i32_e32 v68, v96
	v_cvt_f32_i32_e32 v73, v93
	v_cvt_f32_i32_e32 v72, v92
	v_med3_f32 v84, v84, s54, v210
	v_pk_mul_f32 v[68:69], v[76:77], v[68:69]
	v_med3_f32 v85, v85, s54, v210
	v_pk_fma_f32 v[68:69], v[68:69], v[224:225], v[66:67] op_sel_hi:[1,0,1]
	v_pk_mul_f32 v[72:73], v[80:81], v[72:73]
	v_min_f32_e32 v68, 0x40e00000, v68
	v_min_f32_e32 v69, 0x40e00000, v69
	v_pk_mul_f32 v[90:91], v[68:69], s[12:13] op_sel_hi:[1,0]
	v_pk_fma_f32 v[72:73], v[72:73], v[224:225], v[180:181] op_sel_hi:[1,0,1]
	v_exp_f32_e32 v90, v90
	v_exp_f32_e32 v91, v91
	v_med3_f32 v72, v72, s54, v210
	v_med3_f32 v73, v73, s54, v210
	v_pk_fma_f32 v[90:91], v[90:91], s[14:15], s[14:15] op_sel_hi:[1,0,0]
	s_nop 0
	v_rcp_f32_e32 v90, v90
	v_rcp_f32_e32 v91, v91
	s_nop 0
	v_pk_mul_f32 v[68:69], v[68:69], v[90:91]
	s_nop 0
	v_pk_mul_f32 v[68:69], v[72:73], v[68:69]
	v_cvt_f32_i32_e32 v73, v87
	v_cvt_f32_i32_e32 v72, v86
	v_pk_mul_f32 v[72:73], v[50:51], v[72:73]
	s_nop 0
	v_pk_fma_f32 v[72:73], v[72:73], v[224:225], v[46:47] op_sel_hi:[1,0,1]
	s_nop 0
	v_min_f32_e32 v72, 0x40e00000, v72
	v_min_f32_e32 v73, 0x40e00000, v73
	v_pk_mul_f32 v[86:87], v[72:73], s[12:13] op_sel_hi:[1,0]
	s_nop 0
	v_exp_f32_e32 v86, v86
	v_exp_f32_e32 v87, v87
	s_nop 0
	v_pk_fma_f32 v[86:87], v[86:87], s[14:15], s[14:15] op_sel_hi:[1,0,0]
	s_nop 0
	v_rcp_f32_e32 v86, v86
	v_rcp_f32_e32 v87, v87
	s_nop 0
	v_pk_mul_f32 v[72:73], v[72:73], v[86:87]
	s_nop 0
	v_pk_mul_f32 v[72:73], v[82:83], v[72:73]
	v_cvt_f32_i32_e32 v83, v89
	v_cvt_f32_i32_e32 v82, v88
	v_pk_mul_f32 v[82:83], v[52:53], v[82:83]
	s_nop 0
	v_pk_fma_f32 v[82:83], v[82:83], v[224:225], v[42:43] op_sel_hi:[1,0,1]
	s_nop 0
	v_min_f32_e32 v82, 0x40e00000, v82
	v_min_f32_e32 v83, 0x40e00000, v83
	v_pk_mul_f32 v[86:87], v[82:83], s[12:13] op_sel_hi:[1,0]
	s_waitcnt vmcnt(4)
	v_pk_fma_f32 v[58:59], v[58:59], v[226:227], v[182:183] op_sel_hi:[1,0,1]
	v_exp_f32_e32 v86, v86
	v_exp_f32_e32 v87, v87
	v_med3_f32 v58, v58, s54, v210
	v_med3_f32 v59, v59, s54, v210
	v_pk_fma_f32 v[60:61], v[60:61], v[226:227], v[180:181] op_sel_hi:[1,0,1]
	v_pk_fma_f32 v[86:87], v[86:87], s[14:15], s[14:15] op_sel_hi:[1,0,0]
	v_pk_fma_f32 v[38:39], v[38:39], v[226:227], v[46:47] op_sel_hi:[1,0,1]
	v_rcp_f32_e32 v86, v86
	v_rcp_f32_e32 v87, v87
	v_med3_f32 v60, v60, s54, v210
	v_med3_f32 v61, v61, s54, v210
	v_min_f32_e32 v38, 0x40e00000, v38
	v_pk_mul_f32 v[82:83], v[82:83], v[86:87]
	v_min_f32_e32 v39, 0x40e00000, v39
	v_pk_mul_f32 v[84:85], v[84:85], v[82:83]
	v_mov_b32_e32 v82, v167
	v_cvt_pk_fp8_f32 v82, v48, v49
	v_cvt_f32_i32_e32 v49, v63
	v_cvt_f32_i32_e32 v48, v62
	v_pk_fma_f32 v[22:23], v[22:23], v[226:227], v[178:179] op_sel_hi:[1,0,1]
	v_mov_b32_e32 v83, v167
	v_med3_f32 v22, v22, s54, v210
	v_pk_mul_f32 v[48:49], v[74:75], v[48:49]
	v_med3_f32 v23, v23, s54, v210
	v_pk_fma_f32 v[48:49], v[48:49], v[226:227], v[70:71] op_sel_hi:[1,0,1]
	v_cvt_pk_fp8_f32 v83, v72, v73
	v_min_f32_e32 v48, 0x40e00000, v48
	v_min_f32_e32 v49, 0x40e00000, v49
	v_pk_mul_f32 v[62:63], v[48:49], s[12:13] op_sel_hi:[1,0]
	v_cvt_pk_fp8_f32 v83, v84, v85 op_sel:[0,0,1]
	v_exp_f32_e32 v62, v62
	v_exp_f32_e32 v63, v63
	v_mov_b32_e32 v84, v167
	v_mov_b32_e32 v85, v167
	v_pk_fma_f32 v[24:25], v[24:25], v[226:227], v[176:177] op_sel_hi:[1,0,1]
	v_pk_fma_f32 v[62:63], v[62:63], s[14:15], s[14:15] op_sel_hi:[1,0,0]
	v_med3_f32 v24, v24, s54, v210
	v_rcp_f32_e32 v62, v62
	v_rcp_f32_e32 v63, v63
	v_med3_f32 v25, v25, s54, v210
	v_cvt_pk_fp8_f32 v82, v68, v69 op_sel:[0,0,1]
	v_pk_mul_f32 v[48:49], v[48:49], v[62:63]
	s_nop 0
	v_pk_mul_f32 v[48:49], v[58:59], v[48:49]
	v_cvt_f32_i32_e32 v59, v65
	v_cvt_f32_i32_e32 v58, v64
	v_cvt_pk_fp8_f32 v84, v48, v49
	v_pk_mul_f32 v[58:59], v[76:77], v[58:59]
	s_nop 0
	v_pk_fma_f32 v[58:59], v[58:59], v[226:227], v[66:67] op_sel_hi:[1,0,1]
	s_nop 0
	v_min_f32_e32 v58, 0x40e00000, v58
	v_min_f32_e32 v59, 0x40e00000, v59
	v_pk_mul_f32 v[62:63], v[58:59], s[12:13] op_sel_hi:[1,0]
	s_nop 0
	v_exp_f32_e32 v62, v62
	v_exp_f32_e32 v63, v63
	s_nop 0
	v_pk_fma_f32 v[62:63], v[62:63], s[14:15], s[14:15] op_sel_hi:[1,0,0]
	s_nop 0
	v_rcp_f32_e32 v62, v62
	v_rcp_f32_e32 v63, v63
	s_nop 0
	v_pk_mul_f32 v[58:59], v[58:59], v[62:63]
	s_nop 0
	v_pk_mul_f32 v[58:59], v[60:61], v[58:59]
	v_pk_mul_f32 v[60:61], v[38:39], s[12:13] op_sel_hi:[1,0]
	v_cvt_pk_fp8_f32 v84, v58, v59 op_sel:[0,0,1]
	v_exp_f32_e32 v60, v60
	v_exp_f32_e32 v61, v61
	v_permlane16_swap_b32_e32 v82, v84
	v_pk_fma_f32 v[60:61], v[60:61], s[14:15], s[14:15] op_sel_hi:[1,0,0]
	s_nop 0
	v_rcp_f32_e32 v60, v60
	v_rcp_f32_e32 v61, v61
	s_nop 0
	v_pk_mul_f32 v[38:39], v[38:39], v[60:61]
	s_nop 0
	v_pk_mul_f32 v[22:23], v[22:23], v[38:39]
	v_cvt_f32_i32_e32 v39, v41
	v_cvt_f32_i32_e32 v38, v40
	v_cvt_pk_fp8_f32 v85, v22, v23
	v_or_b32_e32 v22, v45, v191
	v_ashrrev_i32_e32 v23, 31, v22
	v_pk_mul_f32 v[38:39], v[52:53], v[38:39]
	v_lshlrev_b64 v[22:23], 10, v[22:23]
	v_pk_fma_f32 v[38:39], v[38:39], v[226:227], v[42:43] op_sel_hi:[1,0,1]
	v_lshl_add_u64 v[22:23], s[94:95], 0, v[22:23]
	v_min_f32_e32 v38, 0x40e00000, v38
	v_min_f32_e32 v39, 0x40e00000, v39
	v_pk_mul_f32 v[40:41], v[38:39], s[12:13] op_sel_hi:[1,0]
	v_lshl_add_u64 v[22:23], v[22:23], 0, v[172:173]
	v_exp_f32_e32 v40, v40
	v_exp_f32_e32 v41, v41
	s_nop 0
	v_pk_fma_f32 v[40:41], v[40:41], s[14:15], s[14:15] op_sel_hi:[1,0,0]
	s_nop 0
	v_rcp_f32_e32 v40, v40
	v_rcp_f32_e32 v41, v41
	s_nop 0
	v_pk_mul_f32 v[38:39], v[38:39], v[40:41]
	s_nop 0
	v_pk_mul_f32 v[24:25], v[24:25], v[38:39]
	s_nop 0
	v_cvt_pk_fp8_f32 v85, v24, v25 op_sel:[0,0,1]
	v_cvt_f32_i32_e32 v25, v27
	v_cvt_f32_i32_e32 v24, v26
	v_cvt_f32_i32_e32 v27, v35
	v_permlane16_swap_b32_e32 v83, v85
	global_store_dwordx4 v[22:23], v[82:85], off
	s_nop 0
	v_pk_mul_f32 v[24:25], v[74:75], v[24:25]
	v_cvt_f32_i32_e32 v26, v34
	v_pk_mul_f32 v[26:27], v[78:79], v[26:27]
	s_waitcnt vmcnt(4)
	v_pk_fma_f32 v[24:25], v[24:25], v[228:229], v[70:71] op_sel_hi:[1,0,1]
	s_nop 0
	v_min_f32_e32 v24, 0x40e00000, v24
	v_min_f32_e32 v25, 0x40e00000, v25
	v_pk_mul_f32 v[34:35], v[24:25], s[12:13] op_sel_hi:[1,0]
	v_pk_fma_f32 v[26:27], v[26:27], v[228:229], v[182:183] op_sel_hi:[1,0,1]
	v_exp_f32_e32 v34, v34
	v_exp_f32_e32 v35, v35
	v_med3_f32 v26, v26, s54, v210
	v_med3_f32 v27, v27, s54, v210
	v_pk_fma_f32 v[18:19], v[18:19], v[228:229], v[46:47] op_sel_hi:[1,0,1]
	v_pk_fma_f32 v[34:35], v[34:35], s[14:15], s[14:15] op_sel_hi:[1,0,0]
	v_min_f32_e32 v18, 0x40e00000, v18
	v_rcp_f32_e32 v34, v34
	v_rcp_f32_e32 v35, v35
	v_min_f32_e32 v19, 0x40e00000, v19
	v_pk_mul_f32 v[24:25], v[24:25], v[34:35]
	s_nop 0
	v_pk_mul_f32 v[24:25], v[26:27], v[24:25]
	v_cvt_f32_i32_e32 v27, v29
	v_cvt_f32_i32_e32 v26, v28
	v_cvt_f32_i32_e32 v29, v37
	v_cvt_f32_i32_e32 v28, v36
	v_pk_mul_f32 v[26:27], v[76:77], v[26:27]
	s_nop 0
	v_pk_fma_f32 v[26:27], v[26:27], v[228:229], v[66:67] op_sel_hi:[1,0,1]
	v_pk_mul_f32 v[28:29], v[80:81], v[28:29]
	v_min_f32_e32 v26, 0x40e00000, v26
	v_min_f32_e32 v27, 0x40e00000, v27
	v_pk_mul_f32 v[34:35], v[26:27], s[12:13] op_sel_hi:[1,0]
	v_pk_fma_f32 v[28:29], v[28:29], v[228:229], v[180:181] op_sel_hi:[1,0,1]
	v_exp_f32_e32 v34, v34
	v_exp_f32_e32 v35, v35
	v_med3_f32 v28, v28, s54, v210
	v_med3_f32 v29, v29, s54, v210
	v_pk_fma_f32 v[34:35], v[34:35], s[14:15], s[14:15] op_sel_hi:[1,0,0]
	s_nop 0
	v_rcp_f32_e32 v34, v34
	v_rcp_f32_e32 v35, v35
	s_nop 0
	v_pk_mul_f32 v[26:27], v[26:27], v[34:35]
	s_nop 0
	v_pk_mul_f32 v[26:27], v[28:29], v[26:27]
	v_cvt_f32_i32_e32 v29, v31
	v_cvt_f32_i32_e32 v28, v30
	v_pk_mul_f32 v[30:31], v[18:19], s[12:13] op_sel_hi:[1,0]
	v_pk_mul_f32 v[28:29], v[54:55], v[28:29]
	v_exp_f32_e32 v30, v30
	v_exp_f32_e32 v31, v31
	v_pk_fma_f32 v[28:29], v[28:29], v[228:229], v[178:179] op_sel_hi:[1,0,1]
	v_pk_fma_f32 v[30:31], v[30:31], s[14:15], s[14:15] op_sel_hi:[1,0,0]
	s_nop 0
	v_rcp_f32_e32 v30, v30
	v_rcp_f32_e32 v31, v31
	v_med3_f32 v28, v28, s54, v210
	v_med3_f32 v29, v29, s54, v210
	v_pk_mul_f32 v[18:19], v[18:19], v[30:31]
	s_nop 0
	v_pk_mul_f32 v[28:29], v[28:29], v[18:19]
	v_cvt_f32_i32_e32 v19, v21
	v_cvt_f32_i32_e32 v18, v20
	v_cvt_f32_i32_e32 v21, v33
	v_cvt_f32_i32_e32 v20, v32
	v_pk_mul_f32 v[18:19], v[52:53], v[18:19]
	s_nop 0
	v_pk_fma_f32 v[18:19], v[18:19], v[228:229], v[42:43] op_sel_hi:[1,0,1]
	v_pk_mul_f32 v[20:21], v[56:57], v[20:21]
	v_min_f32_e32 v18, 0x40e00000, v18
	v_min_f32_e32 v19, 0x40e00000, v19
	v_pk_fma_f32 v[20:21], v[20:21], v[228:229], v[176:177] op_sel_hi:[1,0,1]
	v_pk_mul_f32 v[22:23], v[18:19], s[12:13] op_sel_hi:[1,0]
	v_med3_f32 v20, v20, s54, v210
	v_exp_f32_e32 v22, v22
	v_exp_f32_e32 v23, v23
	v_med3_f32 v21, v21, s54, v210
	v_pk_fma_f32 v[22:23], v[22:23], s[14:15], s[14:15] op_sel_hi:[1,0,0]
	s_nop 0
	v_rcp_f32_e32 v22, v22
	v_rcp_f32_e32 v23, v23
	s_nop 0
	v_pk_mul_f32 v[18:19], v[18:19], v[22:23]
	s_nop 0
	v_pk_mul_f32 v[20:21], v[20:21], v[18:19]
	v_mov_b32_e32 v19, v167
	v_cvt_pk_fp8_f32 v19, v28, v29
	v_mov_b32_e32 v18, v167
	v_cvt_pk_fp8_f32 v18, v24, v25
	v_cvt_pk_fp8_f32 v19, v20, v21 op_sel:[0,0,1]
	s_nop 0
	v_cvt_pk_fp8_f32 v18, v26, v27 op_sel:[0,0,1]
	s_waitcnt vmcnt(3)
	v_pk_fma_f32 v[10:11], v[10:11], v[230:231], v[70:71] op_sel_hi:[1,0,1]
	s_nop 0
	v_min_f32_e32 v10, 0x40e00000, v10
	v_min_f32_e32 v11, 0x40e00000, v11
	v_pk_mul_f32 v[22:23], v[10:11], s[12:13] op_sel_hi:[1,0]
	v_pk_fma_f32 v[14:15], v[14:15], v[230:231], v[182:183] op_sel_hi:[1,0,1]
	v_exp_f32_e32 v22, v22
	v_exp_f32_e32 v23, v23
	v_pk_fma_f32 v[12:13], v[12:13], v[230:231], v[66:67] op_sel_hi:[1,0,1]
	v_med3_f32 v14, v14, s54, v210
	v_med3_f32 v15, v15, s54, v210
	v_pk_fma_f32 v[22:23], v[22:23], s[14:15], s[14:15] op_sel_hi:[1,0,0]
	v_min_f32_e32 v12, 0x40e00000, v12
	v_rcp_f32_e32 v22, v22
	v_rcp_f32_e32 v23, v23
	v_min_f32_e32 v13, 0x40e00000, v13
	v_pk_fma_f32 v[2:3], v[2:3], v[230:231], v[46:47] op_sel_hi:[1,0,1]
	v_pk_fma_f32 v[6:7], v[6:7], v[230:231], v[178:179] op_sel_hi:[1,0,1]
	v_pk_mul_f32 v[10:11], v[10:11], v[22:23]
	v_min_f32_e32 v2, 0x40e00000, v2
	v_pk_mul_f32 v[10:11], v[14:15], v[10:11]
	v_cvt_f32_i32_e32 v15, v17
	v_cvt_f32_i32_e32 v14, v16
	v_pk_mul_f32 v[16:17], v[12:13], s[12:13] op_sel_hi:[1,0]
	v_min_f32_e32 v3, 0x40e00000, v3
	v_exp_f32_e32 v16, v16
	v_exp_f32_e32 v17, v17
	v_pk_mul_f32 v[14:15], v[80:81], v[14:15]
	v_pk_fma_f32 v[4:5], v[4:5], v[230:231], v[42:43] op_sel_hi:[1,0,1]
	v_pk_fma_f32 v[14:15], v[14:15], v[230:231], v[180:181] op_sel_hi:[1,0,1]
	v_pk_fma_f32 v[16:17], v[16:17], s[14:15], s[14:15] op_sel_hi:[1,0,0]
	v_med3_f32 v14, v14, s54, v210
	v_rcp_f32_e32 v16, v16
	v_rcp_f32_e32 v17, v17
	v_med3_f32 v15, v15, s54, v210
	v_med3_f32 v6, v6, s54, v210
	v_med3_f32 v7, v7, s54, v210
	v_pk_mul_f32 v[12:13], v[12:13], v[16:17]
	v_min_f32_e32 v4, 0x40e00000, v4
	v_pk_mul_f32 v[12:13], v[14:15], v[12:13]
	v_pk_mul_f32 v[14:15], v[2:3], s[12:13] op_sel_hi:[1,0]
	v_min_f32_e32 v5, 0x40e00000, v5
	v_exp_f32_e32 v14, v14
	v_exp_f32_e32 v15, v15
	s_nop 0
	v_pk_fma_f32 v[14:15], v[14:15], s[14:15], s[14:15] op_sel_hi:[1,0,0]
	s_nop 0
	v_rcp_f32_e32 v14, v14
	v_rcp_f32_e32 v15, v15
	s_nop 0
	v_pk_mul_f32 v[2:3], v[2:3], v[14:15]
	s_nop 0
	v_pk_mul_f32 v[2:3], v[6:7], v[2:3]
	v_cvt_f32_i32_e32 v7, v9
	v_cvt_f32_i32_e32 v6, v8
	v_pk_mul_f32 v[8:9], v[4:5], s[12:13] op_sel_hi:[1,0]
	v_pk_mul_f32 v[6:7], v[56:57], v[6:7]
	v_exp_f32_e32 v8, v8
	v_exp_f32_e32 v9, v9
	v_pk_fma_f32 v[6:7], v[6:7], v[230:231], v[176:177] op_sel_hi:[1,0,1]
	v_mov_b32_e32 v20, v167
	v_mov_b32_e32 v21, v167
	v_pk_fma_f32 v[8:9], v[8:9], s[14:15], s[14:15] op_sel_hi:[1,0,0]
	v_cvt_pk_fp8_f32 v20, v10, v11
	v_rcp_f32_e32 v8, v8
	v_rcp_f32_e32 v9, v9
	v_cvt_pk_fp8_f32 v21, v2, v3
	v_med3_f32 v6, v6, s54, v210
	v_med3_f32 v7, v7, s54, v210
	v_pk_mul_f32 v[4:5], v[4:5], v[8:9]
	v_cvt_pk_fp8_f32 v20, v12, v13 op_sel:[0,0,1]
	v_pk_mul_f32 v[4:5], v[6:7], v[4:5]
	v_or_b32_e32 v2, v45, v192
	v_cvt_pk_fp8_f32 v21, v4, v5 op_sel:[0,0,1]
	v_ashrrev_i32_e32 v3, 31, v2
	v_lshlrev_b64 v[2:3], 10, v[2:3]
	v_lshl_add_u64 v[2:3], s[94:95], 0, v[2:3]
	v_permlane16_swap_b32_e32 v18, v20
	v_permlane16_swap_b32_e32 v19, v21
	v_lshl_add_u64 v[2:3], v[2:3], 0, v[172:173]
	global_store_dwordx4 v[2:3], v[18:21], off
	s_cbranch_vccnz .LBB0_497
	s_andn2_b64 vcc, exec, s[4:5]
	s_cbranch_vccnz .LBB0_496
	s_barrier
	s_branch .LBB0_496
